# router RMSNorm loop: all eight row loads issued together
# speedup vs baseline: 1.0039x; 1.0039x over previous
; #define LAS __attribute__((address_space(3)))
; __device__ __forceinline__ unsigned pk2(float lo, float hi) { return f2bf(lo) | (f2bf(hi) << 16); }
; __device__ __forceinline__ float rms_row_load(const float* xrow, int lane, f32x4 (&v)[8]) {
;     const f32x4* xr = (const f32x4*)xrow + lane; float s = 0.f;
; #pragma unroll
;     for (int j = 0; j < 8; ++j) { v[j] = xr[64 * j]; s += (v[j].x * v[j].x + v[j].y * v[j].y) + (v[j].z * v[j].z + v[j].w * v[j].w); }
;     return 1.0f / sqrtf(wave_sum(s) * (1.0f / D) + EPS);
; __global__ void __launch_bounds__(NWAVES * 64, 2) trunk_fwd(Args args) {
;     ...
;                     f32x4 v[8]; const float rstd = rms_row_load(XA + (size_t)m * D, lane, v);
;                     const f32x4* gr = (const f32x4*)gain + lane; unsigned long long* o8 = (unsigned long long*)(Hb + (size_t)m * D) + lane;
;                     float lg[8];
; #pragma unroll
;                     for (int e = 0; e < 8; ++e) lg[e] = 0.f;
; #pragma unroll
;                     for (int jj = 0; jj < 8; ++jj) { const f32x4 gg = gr[64 * jj]; const float a0 = v[jj].x * rstd * gg.x, a1 = v[jj].y * rstd * gg.y, a2 = v[jj].z * rstd * gg.z, a3 = v[jj].w * rstd * gg.w;
;                         o8[64 * jj] = (unsigned long long)pk2(a0, a1) | ((unsigned long long)pk2(a2, a3) << 32);
;                         const int c0 = 256 * jj + 4 * lane; const float av[4] = {a0, a1, a2, a3};
; #pragma unroll
;                         for (int q = 0; q < 4; ++q) { const f32x4 w0 = *(const LAS f32x4*)(RW + (c0 + q) * 8), w1 = *(const LAS f32x4*)(RW + (c0 + q) * 8 + 4);
;                             lg[0] += av[q] * w0.x; lg[1] += av[q] * w0.y; lg[2] += av[q] * w0.z; lg[3] += av[q] * w0.w; lg[4] += av[q] * w1.x; lg[5] += av[q] * w1.y; lg[6] += av[q] * w1.z; lg[7] += av[q] * w1.w; } }
.LBB0_770:
	v_readlane_b32 s4, v250, 6
	v_readlane_b32 s5, v250, 7
	s_mov_b32 s0, 0x36da2000
	s_nop 0
	v_lshl_add_u64 v[2:3], s[4:5], 0, v[56:57]
	v_add_co_u32_e32 v4, vcc, 0x36da1000, v2
	s_nop 1
	v_addc_co_u32_e32 v5, vcc, 0, v3, vcc
	global_load_dwordx4 v[30:33], v[4:5], off
	global_load_dwordx4 v[26:29], v[4:5], off offset:1024
	global_load_dwordx4 v[22:25], v[4:5], off offset:2048
	global_load_dwordx4 v[18:21], v[4:5], off offset:3072
	v_add_co_u32_e32 v2, vcc, s0, v2
	s_mov_b32 s0, 0xf800000
	s_nop 0
	v_addc_co_u32_e32 v3, vcc, 0, v3, vcc
	s_waitcnt lgkmcnt(0)
	global_load_dwordx4 v[14:17], v[2:3], off
	global_load_dwordx4 v[10:13], v[2:3], off offset:1024
	global_load_dwordx4 v[6:9], v[2:3], off offset:2048
	global_load_dwordx4 v[2:5], v[2:3], off offset:3072
	s_waitcnt vmcnt(7)
	v_mul_f32_e32 v34, v31, v31
	v_mul_f32_e32 v133, v33, v33
	v_fmac_f32_e32 v34, v30, v30
	v_fmac_f32_e32 v133, v32, v32
	v_add_f32_e32 v34, v34, v133
	s_waitcnt vmcnt(6)
	v_mul_f32_e32 v132, v27, v27
	v_mul_f32_e32 v133, v29, v29
	v_fmac_f32_e32 v132, v26, v26
	v_fmac_f32_e32 v133, v28, v28
	v_add_f32_e32 v132, v132, v133
	v_add_f32_e32 v34, v34, v132
	s_waitcnt vmcnt(5)
	v_mul_f32_e32 v132, v23, v23
	v_mul_f32_e32 v133, v25, v25
	v_fmac_f32_e32 v132, v22, v22
	v_fmac_f32_e32 v133, v24, v24
	v_add_f32_e32 v132, v132, v133
	v_add_f32_e32 v34, v34, v132
	s_waitcnt vmcnt(4)
	v_mul_f32_e32 v132, v19, v19
	v_mul_f32_e32 v133, v21, v21
	v_fmac_f32_e32 v132, v18, v18
	v_fmac_f32_e32 v133, v20, v20
	v_add_f32_e32 v132, v132, v133
	v_add_f32_e32 v34, v34, v132
	s_waitcnt vmcnt(3)
	v_mul_f32_e32 v132, v15, v15
	v_mul_f32_e32 v133, v17, v17
	v_fmac_f32_e32 v132, v14, v14
	v_fmac_f32_e32 v133, v16, v16
	v_add_f32_e32 v132, v132, v133
	v_add_f32_e32 v34, v34, v132
	s_waitcnt vmcnt(2)
	v_mul_f32_e32 v132, v11, v11
	v_mul_f32_e32 v133, v13, v13
	v_fmac_f32_e32 v132, v10, v10
	v_fmac_f32_e32 v133, v12, v12
	v_add_f32_e32 v132, v132, v133
	v_add_f32_e32 v34, v34, v132
	s_waitcnt vmcnt(1)
	v_mul_f32_e32 v132, v7, v7
	v_mul_f32_e32 v133, v9, v9
	v_fmac_f32_e32 v132, v6, v6
	v_fmac_f32_e32 v133, v8, v8
	v_add_f32_e32 v132, v132, v133
	v_add_f32_e32 v34, v34, v132
	s_waitcnt vmcnt(0)
	v_mul_f32_e32 v132, v3, v3
	v_mul_f32_e32 v133, v5, v5
	v_fmac_f32_e32 v132, v2, v2
	v_fmac_f32_e32 v133, v4, v4
	v_add_f32_e32 v132, v132, v133
	v_add_f32_e32 v34, v34, v132
	ds_bpermute_b32 v35, v43, v34
	s_waitcnt lgkmcnt(0)
	v_add_f32_e32 v34, v34, v35
	ds_bpermute_b32 v35, v63, v34
	s_waitcnt lgkmcnt(0)
	v_add_f32_e32 v34, v34, v35
	ds_bpermute_b32 v35, v65, v34
	s_waitcnt lgkmcnt(0)
	v_add_f32_e32 v34, v34, v35
	ds_bpermute_b32 v35, v67, v34
	s_waitcnt lgkmcnt(0)
	v_add_f32_e32 v34, v34, v35
	ds_bpermute_b32 v35, v69, v34
	s_waitcnt lgkmcnt(0)
	v_add_f32_e32 v34, v34, v35
	ds_bpermute_b32 v35, v71, v34
	s_waitcnt lgkmcnt(0)
	v_add_f32_e32 v34, v34, v35
	v_fmamk_f32 v34, v34, 0x3a000000, v226
	v_cmp_gt_f32_e32 vcc, s0, v34
	v_mul_f32_e32 v35, 0x4f800000, v34
	s_nop 0
	v_cndmask_b32_e32 v34, v34, v35, vcc
	v_sqrt_f32_e32 v35, v34
	s_nop 0
	v_add_u32_e32 v36, -1, v35
	v_fma_f32 v37, -v36, v35, v34
	v_cmp_ge_f32_e64 s[0:1], 0, v37
	v_add_u32_e32 v37, 1, v35
	s_nop 0
	v_cndmask_b32_e64 v36, v35, v36, s[0:1]
	v_fma_f32 v35, -v37, v35, v34
	v_cmp_lt_f32_e64 s[0:1], 0, v35
	s_nop 1
	v_cndmask_b32_e64 v35, v36, v37, s[0:1]
	v_mul_f32_e32 v36, 0x37800000, v35
	v_cndmask_b32_e32 v35, v35, v36, vcc
	v_cmp_class_f32_e32 vcc, v34, v225
	s_nop 1
	v_cndmask_b32_e32 v34, v35, v34, vcc
	v_div_scale_f32 v35, s[0:1], v34, v34, 1.0
	v_rcp_f32_e32 v36, v35
	s_mov_b32 s0, 0x34da1000
	v_fma_f32 v37, -v35, v36, 1.0
	v_fmac_f32_e32 v36, v37, v36
	v_div_scale_f32 v37, vcc, 1.0, v34, 1.0
	v_mul_f32_e32 v38, v37, v36
	v_fma_f32 v39, -v35, v38, v37
	v_fmac_f32_e32 v38, v39, v36
	v_fma_f32 v35, -v35, v38, v37
	v_div_fmas_f32 v35, v35, v36, v38
	v_div_fixup_f32 v80, v35, v34, 1.0
	v_mul_f32_e32 v30, v80, v30
	v_lshl_add_u64 v[34:35], s[4:5], 0, v[54:55]
	v_add_co_u32_e32 v58, vcc, s0, v34
	v_mul_f32_e32 v26, v80, v26
	s_nop 0
	v_addc_co_u32_e32 v59, vcc, 0, v35, vcc
	v_mul_f32_e32 v22, v80, v22
	v_mul_f32_e32 v18, v80, v18
	v_mul_f32_e32 v14, v80, v14
	v_mul_f32_e32 v10, v80, v10
	v_mul_f32_e32 v6, v80, v6
	v_mul_f32_e32 v2, v80, v2
	v_mul_f32_e32 v60, v30, v100
	v_mul_f32_e32 v30, v80, v31
	v_mul_f32_e32 v62, v30, v101
	v_mul_f32_e32 v30, v80, v32
	v_mul_f32_e32 v64, v30, v102
	v_mul_f32_e32 v30, v80, v33
	v_mul_f32_e32 v66, v30, v103
	v_bfe_u32 v30, v60, 16, 1
	v_add3_u32 v30, v60, v30, s36
	v_bfe_u32 v31, v62, 16, 1
	v_lshrrev_b32_e32 v30, 16, v30
	v_add3_u32 v31, v62, v31, s36
	v_and_or_b32 v30, v31, s27, v30
	v_bfe_u32 v31, v64, 16, 1
	v_add3_u32 v31, v64, v31, s36
	v_bfe_u32 v32, v66, 16, 1
	v_lshrrev_b32_e32 v31, 16, v31
	v_add3_u32 v32, v66, v32, s36
	v_and_or_b32 v31, v32, s27, v31
	global_store_dwordx2 v[58:59], v[30:31], off
	ds_read_b128 v[30:33], v73
	ds_read_b128 v[38:41], v73 offset:16
	ds_read_b128 v[34:37], v73 offset:32
	ds_read_b128 v[82:85], v73 offset:48
	s_waitcnt lgkmcnt(3)
	v_fma_f32 v79, v60, v32, 0
	v_fma_f32 v78, v60, v33, 0
	s_waitcnt lgkmcnt(2)
	v_fma_f32 v77, v60, v38, 0
	v_fma_f32 v76, v60, v39, 0
	v_fma_f32 v75, v60, v40, 0
	v_fma_f32 v74, v60, v41, 0
	s_waitcnt lgkmcnt(1)
	v_fmac_f32_e32 v79, v62, v36
	v_fmac_f32_e32 v78, v62, v37
	s_waitcnt lgkmcnt(0)
	v_fmac_f32_e32 v77, v62, v82
	v_fmac_f32_e32 v76, v62, v83
	v_fmac_f32_e32 v75, v62, v84
	v_fmac_f32_e32 v74, v62, v85
	ds_read_b128 v[36:39], v73 offset:64
	ds_read_b128 v[82:85], v73 offset:80
	s_waitcnt lgkmcnt(1)
	v_fmac_f32_e32 v79, v64, v38
	v_fmac_f32_e32 v78, v64, v39
	s_waitcnt lgkmcnt(0)
; #define LAS __attribute__((address_space(3)))
; __device__ __forceinline__ unsigned pk2(float lo, float hi) { return f2bf(lo) | (f2bf(hi) << 16); }
; __global__ void __launch_bounds__(NWAVES * 64, 2) trunk_fwd(Args args) {
;     ...
;                     for (int jj = 0; jj < 8; ++jj) { const f32x4 gg = gr[64 * jj]; const float a0 = v[jj].x * rstd * gg.x, a1 = v[jj].y * rstd * gg.y, a2 = v[jj].z * rstd * gg.z, a3 = v[jj].w * rstd * gg.w;
;                         o8[64 * jj] = (unsigned long long)pk2(a0, a1) | ((unsigned long long)pk2(a2, a3) << 32);
;                         const int c0 = 256 * jj + 4 * lane; const float av[4] = {a0, a1, a2, a3};
; #pragma unroll
;                         for (int q = 0; q < 4; ++q) { const f32x4 w0 = *(const LAS f32x4*)(RW + (c0 + q) * 8), w1 = *(const LAS f32x4*)(RW + (c0 + q) * 8 + 4);
;                             lg[0] += av[q] * w0.x; lg[1] += av[q] * w0.y; lg[2] += av[q] * w0.z; lg[3] += av[q] * w0.w; lg[4] += av[q] * w1.x; lg[5] += av[q] * w1.y; lg[6] += av[q] * w1.z; lg[7] += av[q] * w1.w; } }
	v_fmac_f32_e32 v77, v64, v82
	v_fmac_f32_e32 v76, v64, v83
	v_fmac_f32_e32 v75, v64, v84
	v_fmac_f32_e32 v74, v64, v85
	ds_read_b128 v[38:41], v73 offset:96
	ds_read_b128 v[82:85], v73 offset:112
	s_waitcnt lgkmcnt(1)
	v_fmac_f32_e32 v79, v66, v40
	s_waitcnt lgkmcnt(0)
	v_fmac_f32_e32 v77, v66, v82
	v_fmac_f32_e32 v76, v66, v83
	v_fmac_f32_e32 v75, v66, v84
	v_fmac_f32_e32 v74, v66, v85
	v_fmac_f32_e32 v78, v66, v41
	v_mul_f32_e32 v72, v26, v104
	v_mul_f32_e32 v26, v80, v27
	v_mul_f32_e32 v40, v26, v105
	v_mul_f32_e32 v26, v80, v28
	v_mul_f32_e32 v68, v26, v106
	v_mul_f32_e32 v26, v80, v29
	v_mul_f32_e32 v70, v26, v107
	v_bfe_u32 v26, v72, 16, 1
	v_add3_u32 v26, v72, v26, s36
	v_bfe_u32 v27, v40, 16, 1
	v_lshrrev_b32_e32 v26, 16, v26
	v_add3_u32 v27, v40, v27, s36
	v_and_or_b32 v26, v27, s27, v26
	v_bfe_u32 v27, v68, 16, 1
	v_add3_u32 v27, v68, v27, s36
	v_bfe_u32 v28, v70, 16, 1
	v_lshrrev_b32_e32 v27, 16, v27
	v_add3_u32 v28, v70, v28, s36
	v_and_or_b32 v27, v28, s27, v27
	global_store_dwordx2 v[58:59], v[26:27], off offset:512
	v_pk_fma_f32 v[26:27], v[60:61], v[30:31], 0 op_sel_hi:[0,1,0]
	v_pk_fma_f32 v[26:27], v[62:63], v[34:35], v[26:27] op_sel_hi:[0,1,1]
	v_pk_fma_f32 v[26:27], v[64:65], v[36:37], v[26:27] op_sel_hi:[0,1,1]
	v_pk_fma_f32 v[38:39], v[66:67], v[38:39], v[26:27] op_sel_hi:[0,1,1]
	ds_read_b128 v[30:33], v73 offset:8192
	ds_read_b128 v[34:37], v73 offset:8208
	ds_read_b128 v[26:29], v73 offset:8224
	ds_read_b128 v[82:85], v73 offset:8240
	s_waitcnt lgkmcnt(3)
	v_fmac_f32_e32 v79, v72, v32
	v_fmac_f32_e32 v78, v72, v33
	v_pk_fma_f32 v[60:61], v[72:73], v[30:31], v[38:39] op_sel_hi:[0,1,1]
	s_waitcnt lgkmcnt(2)
	v_fmac_f32_e32 v77, v72, v34
	v_fmac_f32_e32 v76, v72, v35
	s_waitcnt lgkmcnt(1)
	v_fmac_f32_e32 v79, v40, v28
	v_fmac_f32_e32 v78, v40, v29
	ds_read_b128 v[28:31], v73 offset:8256
	ds_read_b128 v[32:35], v73 offset:8272
	v_fmac_f32_e32 v75, v72, v36
	v_fmac_f32_e32 v74, v72, v37
	s_waitcnt lgkmcnt(2)
	v_fmac_f32_e32 v77, v40, v82
	v_fmac_f32_e32 v76, v40, v83
	v_fmac_f32_e32 v75, v40, v84
	v_fmac_f32_e32 v74, v40, v85
	s_waitcnt lgkmcnt(1)
	v_fmac_f32_e32 v79, v68, v30
	v_fmac_f32_e32 v78, v68, v31
	s_waitcnt lgkmcnt(0)
	v_fmac_f32_e32 v77, v68, v32
	v_fmac_f32_e32 v76, v68, v33
	v_fmac_f32_e32 v75, v68, v34
	v_fmac_f32_e32 v74, v68, v35
	ds_read_b128 v[30:33], v73 offset:8288
	ds_read_b128 v[34:37], v73 offset:8304
	s_waitcnt lgkmcnt(1)
	v_fmac_f32_e32 v79, v70, v32
	v_fmac_f32_e32 v78, v70, v33
	s_waitcnt lgkmcnt(0)
	v_fmac_f32_e32 v77, v70, v34
	v_fmac_f32_e32 v76, v70, v35
	v_fmac_f32_e32 v75, v70, v36
	v_fmac_f32_e32 v74, v70, v37
	v_mul_f32_e32 v62, v22, v108
	v_mul_f32_e32 v22, v80, v23
	v_mul_f32_e32 v64, v22, v109
	v_mul_f32_e32 v22, v80, v24
	v_mul_f32_e32 v66, v22, v110
	v_mul_f32_e32 v22, v80, v25
	v_mul_f32_e32 v72, v22, v111
	v_bfe_u32 v22, v62, 16, 1
	v_add3_u32 v22, v62, v22, s36
	v_bfe_u32 v23, v64, 16, 1
	v_lshrrev_b32_e32 v22, 16, v22
	v_add3_u32 v23, v64, v23, s36
	v_and_or_b32 v22, v23, s27, v22
	v_bfe_u32 v23, v66, 16, 1
	v_add3_u32 v23, v66, v23, s36
	v_bfe_u32 v24, v72, 16, 1
	v_lshrrev_b32_e32 v23, 16, v23
	v_add3_u32 v24, v72, v24, s36
	v_and_or_b32 v23, v24, s27, v23
	global_store_dwordx2 v[58:59], v[22:23], off offset:1024
	ds_read_b128 v[22:25], v73 offset:16384
	ds_read_b128 v[36:39], v73 offset:16400
	ds_read_b128 v[32:35], v73 offset:16416
	ds_read_b128 v[82:85], v73 offset:16432
	s_waitcnt lgkmcnt(3)
	v_fmac_f32_e32 v79, v62, v24
	v_fmac_f32_e32 v78, v62, v25
	s_waitcnt lgkmcnt(2)
	v_fmac_f32_e32 v77, v62, v36
	v_fmac_f32_e32 v76, v62, v37
	v_fmac_f32_e32 v75, v62, v38
	v_fmac_f32_e32 v74, v62, v39
	s_waitcnt lgkmcnt(1)
	v_fmac_f32_e32 v79, v64, v34
	v_fmac_f32_e32 v78, v64, v35
	s_waitcnt lgkmcnt(0)
	v_fmac_f32_e32 v77, v64, v82
	v_fmac_f32_e32 v76, v64, v83
	v_fmac_f32_e32 v75, v64, v84
	v_fmac_f32_e32 v74, v64, v85
	ds_read_b128 v[34:37], v73 offset:16448
	ds_read_b128 v[82:85], v73 offset:16464
	s_waitcnt lgkmcnt(1)
	v_fmac_f32_e32 v79, v66, v36
	v_fmac_f32_e32 v78, v66, v37
	s_waitcnt lgkmcnt(0)
	v_fmac_f32_e32 v77, v66, v82
	v_fmac_f32_e32 v76, v66, v83
	v_fmac_f32_e32 v75, v66, v84
	v_fmac_f32_e32 v74, v66, v85
	ds_read_b128 v[36:39], v73 offset:16480
	ds_read_b128 v[82:85], v73 offset:16496
	s_waitcnt lgkmcnt(1)
	v_fmac_f32_e32 v79, v72, v38
	s_waitcnt lgkmcnt(0)
	v_fmac_f32_e32 v77, v72, v82
	v_fmac_f32_e32 v76, v72, v83
	v_fmac_f32_e32 v75, v72, v84
	v_fmac_f32_e32 v74, v72, v85
	v_fmac_f32_e32 v78, v72, v39
	v_mul_f32_e32 v24, v18, v112
	v_mul_f32_e32 v18, v80, v19
	v_mul_f32_e32 v38, v18, v113
	v_mul_f32_e32 v18, v80, v20
	v_mul_f32_e32 v96, v18, v114
	v_mul_f32_e32 v18, v80, v21
	v_mul_f32_e32 v98, v18, v115
	v_bfe_u32 v18, v24, 16, 1
	v_add3_u32 v18, v24, v18, s36
	v_bfe_u32 v19, v38, 16, 1
	v_lshrrev_b32_e32 v18, 16, v18
	v_add3_u32 v19, v38, v19, s36
	v_and_or_b32 v18, v19, s27, v18
	v_bfe_u32 v19, v96, 16, 1
	v_add3_u32 v19, v96, v19, s36
	v_bfe_u32 v20, v98, 16, 1
	v_lshrrev_b32_e32 v19, 16, v19
	v_add3_u32 v20, v98, v20, s36
	v_and_or_b32 v19, v20, s27, v19
	global_store_dwordx2 v[58:59], v[18:19], off offset:1536
	ds_read_b128 v[18:21], v73 offset:24576
	ds_read_b128 v[82:85], v73 offset:24592
	ds_read_b128 v[86:89], v73 offset:24608
	ds_read_b128 v[90:93], v73 offset:24624
	s_waitcnt lgkmcnt(3)
	v_fmac_f32_e32 v79, v24, v20
	v_fmac_f32_e32 v78, v24, v21
	s_waitcnt lgkmcnt(2)
	v_fmac_f32_e32 v77, v24, v82
	v_fmac_f32_e32 v76, v24, v83
	v_pk_fma_f32 v[20:21], v[40:41], v[26:27], v[60:61] op_sel_hi:[0,1,1]
	v_fmac_f32_e32 v75, v24, v84
	v_fmac_f32_e32 v74, v24, v85
	s_waitcnt lgkmcnt(1)
	v_fmac_f32_e32 v79, v38, v88
	v_fmac_f32_e32 v78, v38, v89
	s_waitcnt lgkmcnt(0)
; #define LAS __attribute__((address_space(3)))
; __device__ __forceinline__ unsigned pk2(float lo, float hi) { return f2bf(lo) | (f2bf(hi) << 16); }
; __global__ void __launch_bounds__(NWAVES * 64, 2) trunk_fwd(Args args) {
;     ...
;                     for (int jj = 0; jj < 8; ++jj) { const f32x4 gg = gr[64 * jj]; const float a0 = v[jj].x * rstd * gg.x, a1 = v[jj].y * rstd * gg.y, a2 = v[jj].z * rstd * gg.z, a3 = v[jj].w * rstd * gg.w;
;                         o8[64 * jj] = (unsigned long long)pk2(a0, a1) | ((unsigned long long)pk2(a2, a3) << 32);
;                         const int c0 = 256 * jj + 4 * lane; const float av[4] = {a0, a1, a2, a3};
; #pragma unroll
;                         for (int q = 0; q < 4; ++q) { const f32x4 w0 = *(const LAS f32x4*)(RW + (c0 + q) * 8), w1 = *(const LAS f32x4*)(RW + (c0 + q) * 8 + 4);
;                             lg[0] += av[q] * w0.x; lg[1] += av[q] * w0.y; lg[2] += av[q] * w0.z; lg[3] += av[q] * w0.w; lg[4] += av[q] * w1.x; lg[5] += av[q] * w1.y; lg[6] += av[q] * w1.z; lg[7] += av[q] * w1.w; } }
	v_fmac_f32_e32 v77, v38, v90
	v_fmac_f32_e32 v76, v38, v91
	ds_read_b128 v[82:85], v73 offset:24640
	ds_read_b128 v[88:91], v73 offset:24656
	v_pk_fma_f32 v[20:21], v[68:69], v[28:29], v[20:21] op_sel_hi:[0,1,1]
	v_pk_fma_f32 v[20:21], v[70:71], v[30:31], v[20:21] op_sel_hi:[0,1,1]
	v_pk_fma_f32 v[20:21], v[62:63], v[22:23], v[20:21] op_sel_hi:[0,1,1]
	v_pk_fma_f32 v[20:21], v[64:65], v[32:33], v[20:21] op_sel_hi:[0,1,1]
	v_fmac_f32_e32 v75, v38, v92
	v_fmac_f32_e32 v74, v38, v93
	v_pk_fma_f32 v[20:21], v[66:67], v[34:35], v[20:21] op_sel_hi:[0,1,1]
	s_waitcnt lgkmcnt(0)
	v_fmac_f32_e32 v77, v96, v88
	v_fmac_f32_e32 v76, v96, v89
	v_fmac_f32_e32 v75, v96, v90
	v_fmac_f32_e32 v74, v96, v91
	ds_read_b128 v[88:91], v73 offset:24672
	ds_read_b128 v[92:95], v73 offset:24688
	v_pk_fma_f32 v[20:21], v[72:73], v[36:37], v[20:21] op_sel_hi:[0,1,1]
	v_pk_fma_f32 v[18:19], v[24:25], v[18:19], v[20:21] op_sel_hi:[0,1,1]
	v_pk_fma_f32 v[18:19], v[38:39], v[86:87], v[18:19] op_sel_hi:[0,1,1]
	v_pk_fma_f32 v[18:19], v[96:97], v[82:83], v[18:19] op_sel_hi:[0,1,1]
	s_waitcnt lgkmcnt(1)
	v_pk_fma_f32 v[32:33], v[98:99], v[88:89], v[18:19] op_sel_hi:[0,1,1]
	v_fmac_f32_e32 v79, v96, v84
	v_fmac_f32_e32 v78, v96, v85
	v_fmac_f32_e32 v79, v98, v90
	v_fmac_f32_e32 v78, v98, v91
	s_waitcnt lgkmcnt(0)
	v_fmac_f32_e32 v77, v98, v92
	v_fmac_f32_e32 v76, v98, v93
	v_fmac_f32_e32 v75, v98, v94
	v_fmac_f32_e32 v74, v98, v95
	v_mul_f32_e32 v34, v14, v116
	v_mul_f32_e32 v14, v80, v15
	v_mul_f32_e32 v36, v14, v117
	v_mul_f32_e32 v14, v80, v16
	v_mul_f32_e32 v38, v14, v118
	v_mul_f32_e32 v14, v80, v17
	v_mul_f32_e32 v40, v14, v119
	v_bfe_u32 v14, v34, 16, 1
	v_add3_u32 v14, v34, v14, s36
	v_bfe_u32 v15, v36, 16, 1
	v_lshrrev_b32_e32 v14, 16, v14
	v_add3_u32 v15, v36, v15, s36
	v_and_or_b32 v14, v15, s27, v14
	v_bfe_u32 v15, v38, 16, 1
	v_add3_u32 v15, v38, v15, s36
	v_bfe_u32 v16, v40, 16, 1
	v_lshrrev_b32_e32 v15, 16, v15
	v_add3_u32 v16, v40, v16, s36
	v_and_or_b32 v15, v16, s27, v15
	global_store_dwordx2 v[58:59], v[14:15], off offset:2048
	ds_read_b128 v[14:17], v73 offset:32768
	ds_read_b128 v[22:25], v73 offset:32784
	ds_read_b128 v[18:21], v73 offset:32800
	ds_read_b128 v[26:29], v73 offset:32816
	s_waitcnt lgkmcnt(3)
	v_fmac_f32_e32 v79, v34, v16
	v_fmac_f32_e32 v78, v34, v17
	s_waitcnt lgkmcnt(2)
	v_fmac_f32_e32 v77, v34, v22
	v_fmac_f32_e32 v76, v34, v23
	v_fmac_f32_e32 v75, v34, v24
	v_fmac_f32_e32 v74, v34, v25
	s_waitcnt lgkmcnt(1)
	v_fmac_f32_e32 v79, v36, v20
	v_fmac_f32_e32 v78, v36, v21
	s_waitcnt lgkmcnt(0)
	v_fmac_f32_e32 v77, v36, v26
	v_fmac_f32_e32 v76, v36, v27
	ds_read_b128 v[20:23], v73 offset:32832
	ds_read_b128 v[24:27], v73 offset:32848
	v_fmac_f32_e32 v75, v36, v28
	v_fmac_f32_e32 v74, v36, v29
	s_waitcnt lgkmcnt(1)
	v_fmac_f32_e32 v79, v38, v22
	v_fmac_f32_e32 v78, v38, v23
	s_waitcnt lgkmcnt(0)
	v_fmac_f32_e32 v77, v38, v24
	v_fmac_f32_e32 v76, v38, v25
	v_fmac_f32_e32 v75, v38, v26
	v_fmac_f32_e32 v74, v38, v27
	ds_read_b128 v[22:25], v73 offset:32864
	ds_read_b128 v[26:29], v73 offset:32880
	s_waitcnt lgkmcnt(1)
	v_fmac_f32_e32 v79, v40, v24
	v_fmac_f32_e32 v78, v40, v25
	s_waitcnt lgkmcnt(0)
	v_fmac_f32_e32 v77, v40, v26
	v_fmac_f32_e32 v76, v40, v27
	v_fmac_f32_e32 v75, v40, v28
	v_fmac_f32_e32 v74, v40, v29
	v_mul_f32_e32 v60, v10, v120
	v_mul_f32_e32 v10, v80, v11
	v_mul_f32_e32 v62, v10, v121
	v_mul_f32_e32 v10, v80, v12
	v_mul_f32_e32 v64, v10, v122
	v_mul_f32_e32 v10, v80, v13
	v_mul_f32_e32 v66, v10, v123
	v_bfe_u32 v10, v60, 16, 1
	v_add3_u32 v10, v60, v10, s36
	v_bfe_u32 v11, v62, 16, 1
	v_lshrrev_b32_e32 v10, 16, v10
	v_add3_u32 v11, v62, v11, s36
	v_and_or_b32 v10, v11, s27, v10
	v_bfe_u32 v11, v64, 16, 1
	v_add3_u32 v11, v64, v11, s36
	v_bfe_u32 v12, v66, 16, 1
	v_lshrrev_b32_e32 v11, 16, v11
	v_add3_u32 v12, v66, v12, s36
	v_and_or_b32 v11, v12, s27, v11
	global_store_dwordx2 v[58:59], v[10:11], off offset:2560
	ds_read_b128 v[10:13], v73 offset:40960
	ds_read_b128 v[28:31], v73 offset:40976
	ds_read_b128 v[24:27], v73 offset:40992
	ds_read_b128 v[82:85], v73 offset:41008
	s_waitcnt lgkmcnt(3)
	v_fmac_f32_e32 v79, v60, v12
	v_fmac_f32_e32 v78, v60, v13
	s_waitcnt lgkmcnt(2)
	v_fmac_f32_e32 v77, v60, v28
	v_fmac_f32_e32 v76, v60, v29
	v_fmac_f32_e32 v75, v60, v30
	v_fmac_f32_e32 v74, v60, v31
	s_waitcnt lgkmcnt(1)
	v_fmac_f32_e32 v79, v62, v26
	v_fmac_f32_e32 v78, v62, v27
	s_waitcnt lgkmcnt(0)
	v_fmac_f32_e32 v77, v62, v82
	v_fmac_f32_e32 v76, v62, v83
	v_fmac_f32_e32 v75, v62, v84
	v_fmac_f32_e32 v74, v62, v85
	ds_read_b128 v[26:29], v73 offset:41024
	ds_read_b128 v[82:85], v73 offset:41040
	s_waitcnt lgkmcnt(1)
	v_fmac_f32_e32 v79, v64, v28
	v_fmac_f32_e32 v78, v64, v29
	s_waitcnt lgkmcnt(0)
	v_fmac_f32_e32 v77, v64, v82
	v_fmac_f32_e32 v76, v64, v83
	v_fmac_f32_e32 v75, v64, v84
	v_fmac_f32_e32 v74, v64, v85
	ds_read_b128 v[28:31], v73 offset:41056
	ds_read_b128 v[82:85], v73 offset:41072
	s_waitcnt lgkmcnt(1)
	v_fmac_f32_e32 v79, v66, v30
	s_waitcnt lgkmcnt(0)
	v_fmac_f32_e32 v77, v66, v82
	v_fmac_f32_e32 v76, v66, v83
	v_fmac_f32_e32 v75, v66, v84
	v_fmac_f32_e32 v74, v66, v85
	v_fmac_f32_e32 v78, v66, v31
	v_mul_f32_e32 v12, v6, v124
	v_mul_f32_e32 v6, v80, v7
	v_mul_f32_e32 v7, v80, v9
	v_mul_f32_e32 v30, v6, v125
	v_mul_f32_e32 v16, v7, v127
	v_bfe_u32 v7, v12, 16, 1
	v_mul_f32_e32 v6, v80, v8
	v_add3_u32 v7, v12, v7, s36
	v_bfe_u32 v8, v30, 16, 1
	v_mul_f32_e32 v6, v6, v126
	v_lshrrev_b32_e32 v7, 16, v7
	v_add3_u32 v8, v30, v8, s36
	v_and_or_b32 v8, v8, s27, v7
	v_bfe_u32 v7, v6, 16, 1
	v_add3_u32 v7, v6, v7, s36
	v_bfe_u32 v9, v16, 16, 1
	v_lshrrev_b32_e32 v7, 16, v7
	v_add3_u32 v9, v16, v9, s36
	v_and_or_b32 v9, v9, s27, v7
	global_store_dwordx2 v[58:59], v[8:9], off offset:3072
	ds_read_b128 v[82:85], v73 offset:49152
	ds_read_b128 v[86:89], v73 offset:49168
	ds_read_b128 v[90:93], v73 offset:49184
	ds_read_b128 v[94:97], v73 offset:49200
	v_pk_fma_f32 v[8:9], v[34:35], v[14:15], v[32:33] op_sel_hi:[0,1,1]
	v_pk_fma_f32 v[8:9], v[36:37], v[18:19], v[8:9] op_sel_hi:[0,1,1]
	v_pk_fma_f32 v[8:9], v[38:39], v[20:21], v[8:9] op_sel_hi:[0,1,1]
	v_pk_fma_f32 v[8:9], v[40:41], v[22:23], v[8:9] op_sel_hi:[0,1,1]
	s_waitcnt lgkmcnt(3)
; #define LAS __attribute__((address_space(3)))
; __device__ __forceinline__ unsigned pk2(float lo, float hi) { return f2bf(lo) | (f2bf(hi) << 16); }
; __device__ __forceinline__ float wave_sum(float v) {
; #pragma unroll
;     for (int o = 1; o < 64; o <<= 1) v += __shfl_xor(v, o);
;     return v;
; __global__ void __launch_bounds__(NWAVES * 64, 2) trunk_fwd(Args args) {
;     ...
;                     for (int jj = 0; jj < 8; ++jj) { const f32x4 gg = gr[64 * jj]; const float a0 = v[jj].x * rstd * gg.x, a1 = v[jj].y * rstd * gg.y, a2 = v[jj].z * rstd * gg.z, a3 = v[jj].w * rstd * gg.w;
;                         o8[64 * jj] = (unsigned long long)pk2(a0, a1) | ((unsigned long long)pk2(a2, a3) << 32);
;                         const int c0 = 256 * jj + 4 * lane; const float av[4] = {a0, a1, a2, a3};
; #pragma unroll
;                         for (int q = 0; q < 4; ++q) { const f32x4 w0 = *(const LAS f32x4*)(RW + (c0 + q) * 8), w1 = *(const LAS f32x4*)(RW + (c0 + q) * 8 + 4);
;                             lg[0] += av[q] * w0.x; lg[1] += av[q] * w0.y; lg[2] += av[q] * w0.z; lg[3] += av[q] * w0.w; lg[4] += av[q] * w1.x; lg[5] += av[q] * w1.y; lg[6] += av[q] * w1.z; lg[7] += av[q] * w1.w; } }
; #pragma unroll
;                     for (int e = 0; e < 8; ++e) lg[e] = wave_sum(lg[e]) + args.in[I_RB][e];
;                     if (lane == 0) { int e0 = 0; float v0 = lg[0];
	v_fmac_f32_e32 v79, v12, v84
	v_fmac_f32_e32 v78, v12, v85
	s_waitcnt lgkmcnt(2)
	v_fmac_f32_e32 v77, v12, v86
	v_fmac_f32_e32 v76, v12, v87
	v_pk_fma_f32 v[8:9], v[60:61], v[10:11], v[8:9] op_sel_hi:[0,1,1]
	s_waitcnt lgkmcnt(1)
	v_fmac_f32_e32 v79, v30, v92
	v_fmac_f32_e32 v78, v30, v93
	s_waitcnt lgkmcnt(0)
	v_fmac_f32_e32 v77, v30, v94
	v_fmac_f32_e32 v76, v30, v95
	ds_read_b128 v[84:87], v73 offset:49216
	ds_read_b128 v[92:95], v73 offset:49232
	v_pk_fma_f32 v[8:9], v[62:63], v[24:25], v[8:9] op_sel_hi:[0,1,1]
	v_pk_fma_f32 v[8:9], v[64:65], v[26:27], v[8:9] op_sel_hi:[0,1,1]
	v_pk_fma_f32 v[8:9], v[66:67], v[28:29], v[8:9] op_sel_hi:[0,1,1]
	v_fmac_f32_e32 v75, v12, v88
	v_fmac_f32_e32 v74, v12, v89
	v_pk_fma_f32 v[8:9], v[12:13], v[82:83], v[8:9] op_sel_hi:[0,1,1]
	v_fmac_f32_e32 v75, v30, v96
	v_fmac_f32_e32 v74, v30, v97
	v_pk_fma_f32 v[8:9], v[30:31], v[90:91], v[8:9] op_sel_hi:[0,1,1]
	s_waitcnt lgkmcnt(1)
	v_pk_fma_f32 v[18:19], v[6:7], v[84:85], v[8:9] op_sel_hi:[0,1,1]
	v_fmac_f32_e32 v79, v6, v86
	v_fmac_f32_e32 v78, v6, v87
	s_waitcnt lgkmcnt(0)
	v_fmac_f32_e32 v77, v6, v92
	v_fmac_f32_e32 v76, v6, v93
	v_fmac_f32_e32 v75, v6, v94
	v_fmac_f32_e32 v74, v6, v95
	ds_read_b128 v[6:9], v73 offset:49248
	ds_read_b128 v[10:13], v73 offset:49264
	s_waitcnt lgkmcnt(1)
	v_fmac_f32_e32 v79, v16, v8
	v_fmac_f32_e32 v78, v16, v9
	s_waitcnt lgkmcnt(0)
	v_fmac_f32_e32 v77, v16, v10
	v_fmac_f32_e32 v76, v16, v11
	v_fmac_f32_e32 v75, v16, v12
	v_fmac_f32_e32 v74, v16, v13
	v_mul_f32_e32 v24, v2, v128
	v_mul_f32_e32 v2, v80, v3
	v_mul_f32_e32 v26, v2, v129
	v_mul_f32_e32 v2, v80, v4
	v_mul_f32_e32 v22, v2, v130
	v_mul_f32_e32 v2, v80, v5
	v_mul_f32_e32 v20, v2, v131
	v_bfe_u32 v2, v24, 16, 1
	v_add3_u32 v2, v24, v2, s36
	v_bfe_u32 v3, v26, 16, 1
	v_lshrrev_b32_e32 v2, 16, v2
	v_add3_u32 v3, v26, v3, s36
	v_and_or_b32 v2, v3, s27, v2
	v_bfe_u32 v3, v22, 16, 1
	v_add3_u32 v3, v22, v3, s36
	v_bfe_u32 v4, v20, 16, 1
	v_lshrrev_b32_e32 v3, 16, v3
	v_add3_u32 v4, v20, v4, s36
	v_and_or_b32 v3, v4, s27, v3
	global_store_dwordx2 v[58:59], v[2:3], off offset:3584
	ds_read_b128 v[8:11], v73 offset:57344
	ds_read_b128 v[12:15], v73 offset:57360
	ds_read_b128 v[2:5], v73 offset:57376
	ds_read_b128 v[28:31], v73 offset:57392
	s_waitcnt lgkmcnt(3)
	v_fmac_f32_e32 v79, v24, v10
	s_waitcnt lgkmcnt(2)
	v_fmac_f32_e32 v77, v24, v12
	v_fmac_f32_e32 v76, v24, v13
	v_fmac_f32_e32 v75, v24, v14
	v_fmac_f32_e32 v74, v24, v15
	v_fmac_f32_e32 v78, v24, v11
	s_waitcnt lgkmcnt(0)
	v_fmac_f32_e32 v77, v26, v28
	v_fmac_f32_e32 v76, v26, v29
	v_fmac_f32_e32 v75, v26, v30
	v_fmac_f32_e32 v74, v26, v31
	ds_read_b128 v[10:13], v73 offset:57408
	ds_read_b128 v[28:31], v73 offset:57424
	v_fmac_f32_e32 v79, v26, v4
	v_fmac_f32_e32 v78, v26, v5
	v_pk_fma_f32 v[4:5], v[16:17], v[6:7], v[18:19] op_sel_hi:[0,1,1]
	s_waitcnt lgkmcnt(1)
	v_fmac_f32_e32 v79, v22, v12
	v_fmac_f32_e32 v78, v22, v13
	s_waitcnt lgkmcnt(0)
	v_fmac_f32_e32 v77, v22, v28
	v_fmac_f32_e32 v76, v22, v29
	v_fmac_f32_e32 v75, v22, v30
	v_fmac_f32_e32 v74, v22, v31
	ds_read_b128 v[12:15], v73 offset:57440
	ds_read_b128 v[28:31], v73 offset:57456
	v_pk_fma_f32 v[4:5], v[24:25], v[8:9], v[4:5] op_sel_hi:[0,1,1]
	v_pk_fma_f32 v[2:3], v[26:27], v[2:3], v[4:5] op_sel_hi:[0,1,1]
	v_pk_fma_f32 v[2:3], v[22:23], v[10:11], v[2:3] op_sel_hi:[0,1,1]
	s_waitcnt lgkmcnt(1)
	v_fmac_f32_e32 v78, v20, v15
	ds_bpermute_b32 v8, v43, v78
	s_waitcnt lgkmcnt(1)
	v_fmac_f32_e32 v77, v20, v28
	v_fmac_f32_e32 v76, v20, v29
	v_pk_fma_f32 v[2:3], v[20:21], v[12:13], v[2:3] op_sel_hi:[0,1,1]
	v_fmac_f32_e32 v75, v20, v30
	s_waitcnt lgkmcnt(0)
	v_add_f32_e32 v8, v78, v8
	ds_bpermute_b32 v9, v63, v8
	v_fmac_f32_e32 v79, v20, v14
	v_fmac_f32_e32 v74, v20, v31
	ds_bpermute_b32 v4, v43, v2
	ds_bpermute_b32 v5, v43, v3
	s_waitcnt lgkmcnt(2)
	v_add_f32_e32 v8, v8, v9
	ds_bpermute_b32 v9, v65, v8
	ds_bpermute_b32 v6, v43, v79
	s_waitcnt lgkmcnt(2)
	v_pk_add_f32 v[2:3], v[2:3], v[4:5]
	ds_bpermute_b32 v4, v63, v2
	s_waitcnt lgkmcnt(2)
	v_add_f32_e32 v8, v8, v9
	ds_bpermute_b32 v9, v67, v8
	s_waitcnt lgkmcnt(2)
	v_add_f32_e32 v6, v79, v6
	ds_bpermute_b32 v5, v63, v3
	ds_bpermute_b32 v7, v63, v6
	s_waitcnt lgkmcnt(2)
	v_add_f32_e32 v8, v8, v9
	ds_bpermute_b32 v9, v69, v8
	s_waitcnt lgkmcnt(2)
	v_pk_add_f32 v[2:3], v[2:3], v[4:5]
	s_waitcnt lgkmcnt(1)
	v_add_f32_e32 v6, v6, v7
	ds_bpermute_b32 v4, v65, v2
	ds_bpermute_b32 v5, v65, v3
	s_waitcnt lgkmcnt(2)
	v_add_f32_e32 v9, v8, v9
	ds_bpermute_b32 v8, v43, v77
	ds_bpermute_b32 v7, v65, v6
	ds_bpermute_b32 v10, v71, v9
	s_waitcnt lgkmcnt(3)
	v_pk_add_f32 v[2:3], v[2:3], v[4:5]
	ds_bpermute_b32 v4, v67, v2
	s_waitcnt lgkmcnt(3)
	v_add_f32_e32 v8, v77, v8
	ds_bpermute_b32 v11, v63, v8
	s_waitcnt lgkmcnt(3)
	v_add_f32_e32 v6, v6, v7
	ds_bpermute_b32 v5, v67, v3
	ds_bpermute_b32 v7, v67, v6
	s_waitcnt lgkmcnt(2)
	v_add_f32_e32 v8, v8, v11
	ds_bpermute_b32 v11, v65, v8
	s_waitcnt lgkmcnt(2)
	v_pk_add_f32 v[2:3], v[2:3], v[4:5]
	s_waitcnt lgkmcnt(1)
	v_add_f32_e32 v6, v6, v7
	ds_bpermute_b32 v4, v69, v2
	ds_bpermute_b32 v5, v69, v3
	s_waitcnt lgkmcnt(2)
	v_add_f32_e32 v8, v8, v11
	ds_bpermute_b32 v11, v67, v8
	ds_bpermute_b32 v7, v69, v6
	s_waitcnt lgkmcnt(2)
	v_pk_add_f32 v[2:3], v[2:3], v[4:5]
	ds_bpermute_b32 v4, v71, v2
	s_waitcnt lgkmcnt(2)
	v_add_f32_e32 v8, v8, v11
	ds_bpermute_b32 v11, v69, v8
	s_waitcnt lgkmcnt(2)
	v_add_f32_e32 v6, v6, v7
	ds_bpermute_b32 v5, v71, v3
	ds_bpermute_b32 v7, v71, v6
	s_waitcnt lgkmcnt(2)
	v_add_f32_e32 v12, v8, v11
	ds_bpermute_b32 v8, v43, v76
	ds_bpermute_b32 v13, v71, v12
	s_waitcnt lgkmcnt(1)
	v_add_f32_e32 v8, v76, v8
	ds_bpermute_b32 v11, v63, v8
	s_waitcnt lgkmcnt(0)
	v_add_f32_e32 v8, v8, v11
	ds_bpermute_b32 v11, v65, v8
	s_waitcnt lgkmcnt(0)
	v_add_f32_e32 v8, v8, v11
	ds_bpermute_b32 v11, v67, v8
	s_waitcnt lgkmcnt(0)
	v_add_f32_e32 v8, v8, v11
	ds_bpermute_b32 v11, v69, v8
	s_waitcnt lgkmcnt(0)
	v_add_f32_e32 v14, v8, v11
	ds_bpermute_b32 v8, v43, v75
	ds_bpermute_b32 v15, v71, v14
	s_waitcnt lgkmcnt(1)
	v_add_f32_e32 v8, v75, v8
	ds_bpermute_b32 v11, v63, v8
	s_waitcnt lgkmcnt(0)
	v_add_f32_e32 v8, v8, v11
	ds_bpermute_b32 v11, v65, v8
	s_waitcnt lgkmcnt(0)
	v_add_f32_e32 v8, v8, v11
	ds_bpermute_b32 v11, v67, v8
	s_waitcnt lgkmcnt(0)
	v_add_f32_e32 v8, v8, v11
	ds_bpermute_b32 v11, v69, v8
	s_waitcnt lgkmcnt(0)
	v_add_f32_e32 v11, v8, v11
	ds_bpermute_b32 v8, v43, v74
	ds_bpermute_b32 v16, v71, v11
	s_waitcnt lgkmcnt(1)
	v_add_f32_e32 v8, v74, v8
	ds_bpermute_b32 v17, v63, v8
	s_waitcnt lgkmcnt(0)
	v_add_f32_e32 v8, v8, v17
	ds_bpermute_b32 v17, v65, v8
	s_waitcnt lgkmcnt(0)
	v_add_f32_e32 v8, v8, v17
	ds_bpermute_b32 v17, v67, v8
	s_waitcnt lgkmcnt(0)
	v_add_f32_e32 v8, v8, v17
	ds_bpermute_b32 v17, v69, v8
	s_waitcnt lgkmcnt(0)
	v_add_f32_e32 v8, v8, v17
	ds_bpermute_b32 v17, v71, v8
	s_and_saveexec_b64 s[20:21], s[42:43]
	s_cbranch_execz .LBB0_769
; __global__ void __launch_bounds__(NWAVES * 64, 2) trunk_fwd(Args args) {
;     ...
;                     for (int e = 0; e < 8; ++e) lg[e] = wave_sum(lg[e]) + args.in[I_RB][e];
;                     if (lane == 0) { int e0 = 0; float v0 = lg[0];
; #pragma unroll
;                         for (int e = 1; e < 8; ++e) if (lg[e] > v0) { v0 = lg[e]; e0 = e; }
;                         int e1 = -1; float v1 = -INFINITY;
; #pragma unroll
;                         for (int e = 0; e < 8; ++e) if (e != e0 && lg[e] > v1) { v1 = lg[e]; e1 = e; }
	v_readlane_b32 s44, v255, 7
	v_readlane_b32 s46, v255, 9
	v_readlane_b32 s47, v255, 10
	v_add_f32_e32 v6, v6, v7
	v_pk_add_f32 v[2:3], v[2:3], v[4:5]
	v_add_f32_e32 v9, v9, v10
	v_add_f32_e32 v12, v12, v13
	v_add_f32_e32 v14, v14, v15
	global_load_dwordx4 v[18:21], v187, s[46:47] offset:16
	global_load_dwordx4 v[22:25], v187, s[46:47]
	v_add_f32_e32 v11, v11, v16
	s_waitcnt lgkmcnt(0)
	v_add_f32_e32 v8, v8, v17
	s_mov_b32 s8, 0xff800000
	v_readlane_b32 s45, v255, 8
	v_readlane_b32 s48, v255, 11
	v_readlane_b32 s49, v255, 12
	v_readlane_b32 s50, v255, 13
	v_readlane_b32 s51, v255, 14
	s_waitcnt vmcnt(1)
	v_add_f32_e32 v12, v12, v18
	s_waitcnt vmcnt(0)
	v_add_f32_e32 v10, v6, v24
	v_pk_add_f32 v[6:7], v[2:3], v[22:23]
	v_add_f32_e32 v9, v9, v25
	v_cmp_gt_f32_e32 vcc, v7, v6
	v_add_f32_e32 v14, v14, v19
	v_add_f32_e32 v11, v11, v20
	v_cndmask_b32_e32 v2, v6, v7, vcc
	v_cndmask_b32_e64 v3, 0, 1, vcc
	v_cmp_gt_f32_e32 vcc, v10, v2
	v_add_f32_e32 v8, v8, v21
	v_cmp_nlg_f32_e64 s[8:9], s8, v6
	v_cndmask_b32_e32 v2, v2, v10, vcc
	v_cndmask_b32_e64 v3, v3, 2, vcc
	v_cmp_gt_f32_e32 vcc, v9, v2
	s_nop 1
	v_cndmask_b32_e32 v2, v2, v9, vcc
	v_cndmask_b32_e64 v3, v3, 3, vcc
	v_cmp_gt_f32_e32 vcc, v12, v2
	s_nop 1
	v_cndmask_b32_e32 v2, v2, v12, vcc
	v_cndmask_b32_e64 v3, v3, 4, vcc
	v_cmp_gt_f32_e32 vcc, v14, v2
	s_nop 1
	v_cndmask_b32_e32 v2, v2, v14, vcc
	v_cmp_ngt_f32_e64 s[0:1], v11, v2
	v_cndmask_b32_e64 v3, v3, 5, vcc
	s_nop 0
	v_cndmask_b32_e64 v4, v11, v2, s[0:1]
	v_cndmask_b32_e64 v2, 6, v3, s[0:1]
	v_cmp_gt_f32_e64 s[4:5], v8, v4
	v_cmp_ngt_f32_e32 vcc, v8, v4
	s_nop 0
	v_cndmask_b32_e64 v2, v2, 7, s[4:5]
	v_cmp_eq_u32_e64 s[6:7], 0, v2
	s_or_b64 s[6:7], s[6:7], s[8:9]
	s_or_b64 s[4:5], s[4:5], s[0:1]
	v_cndmask_b32_e64 v3, v6, v229, s[6:7]
	v_cndmask_b32_e64 v5, 0, -1, s[6:7]
	v_cmp_ne_u32_e64 s[6:7], 1, v2
	v_cmp_gt_f32_e64 s[8:9], v7, v3
	s_and_b64 s[6:7], s[6:7], s[8:9]
	v_cndmask_b32_e64 v3, v3, v7, s[6:7]
	v_cndmask_b32_e64 v5, v5, 1, s[6:7]
	v_cmp_ne_u32_e64 s[6:7], 2, v2
	v_cmp_gt_f32_e64 s[8:9], v10, v3
	s_and_b64 s[6:7], s[6:7], s[8:9]
	v_cndmask_b32_e64 v3, v3, v10, s[6:7]
	v_cndmask_b32_e64 v5, v5, 2, s[6:7]
	v_cmp_ne_u32_e64 s[6:7], 3, v2
	v_cmp_gt_f32_e64 s[8:9], v9, v3
	s_and_b64 s[6:7], s[6:7], s[8:9]
	v_cndmask_b32_e64 v3, v3, v9, s[6:7]
	v_cndmask_b32_e64 v5, v5, 3, s[6:7]
	v_cmp_ne_u32_e64 s[6:7], 4, v2
	v_cmp_gt_f32_e64 s[8:9], v12, v3
	s_and_b64 s[6:7], s[6:7], s[8:9]
	v_cndmask_b32_e64 v3, v3, v12, s[6:7]
	v_cndmask_b32_e64 v5, v5, 4, s[6:7]
	v_cmp_ne_u32_e64 s[6:7], 5, v2
	v_cmp_gt_f32_e64 s[8:9], v14, v3
	s_and_b64 s[6:7], s[6:7], s[8:9]
	v_cndmask_b32_e64 v3, v3, v14, s[6:7]
	v_cmp_gt_f32_e64 s[0:1], v11, v3
	v_cndmask_b32_e64 v6, v5, 5, s[6:7]
	s_and_b64 s[0:1], s[4:5], s[0:1]
	v_cndmask_b32_e64 v5, v3, v11, s[0:1]
	v_cndmask_b32_e64 v3, v6, 6, s[0:1]
	s_and_saveexec_b64 s[0:1], vcc
	s_cbranch_execz .LBB0_768
	v_cmp_gt_f32_e32 vcc, v8, v5
	s_and_saveexec_b64 s[4:5], vcc
	s_cbranch_execz .LBB0_767
	v_mov_b32_e32 v3, 7
	v_mov_b32_e32 v5, v8
	s_branch .LBB0_767
